# stack10 with the proj-GEMM K-loop moved by 4 B (MFMA encodings at 4 mod 8, like the up loop), everything after restored by another 4 B
# speedup vs baseline: 1.0047x; 1.0047x over previous
; #define PG8_STAGE(bufoff, gbase, voff) do { _Pragma("unroll") for (int _i = 0; _i < 2; ++_i) \
;         __builtin_amdgcn_global_load_lds((const unsigned*)((const char*)(gbase) + (voff)[_i]), (PG8_LAS unsigned*)(lds + (bufoff) + ldsw + _i * 8192), 16, 0, 0); } while (0)
; #define PG8_WAIT_V(n) asm volatile("s_waitcnt vmcnt(" #n ")" ::: "memory")
; #define PG8_BAR __builtin_amdgcn_s_barrier()
; template <class Epi, class Sched, bool ALIGN_EPI = false, bool SP2 = false>
; __device__ __forceinline__ void gemm_phase(PG8_LAS unsigned char* lds, const Gemm g, const Sched& S, const Epi& E, Stopwatch& sw) {
;     ...
;     for (int i = 0; i < 2; ++i) { int R, C; stage_rc(tid * 16 + i * 8192, R, C); const int Rb = Epi::PERM ? ((R & ~31) + perm32(R & 31)) : R;
;         voffA[i] = (unsigned)(R * K + C) * 2u; voffB[i] = (unsigned)(Rb * K + C) * 2u; }
;     const size_t kstep = (size_t)(BK * 2);
;     const size_t hstep = (size_t)HALF * K * 2;
;     const size_t tstep = 2 * hstep;
;     const unsigned ldsw = (unsigned)wid * 1024u;
;     const int aoff = lds_byte(wr * 64 + fr, fq * 8), boff = lds_byte(wc * 32 + fr, fq * 8);
;     ...
;     const char* cA = (const char*)g.A + (size_t)cur.pm * tstep; const char* cB = (const char*)g.Bt + (size_t)cur.pn * tstep;
;     S.a_ready(cur);
;     if constexpr (SP2) {
;         PG8_STAGE(PG8_SB(0, 0), cB, voffB); PG8_STAGE(PG8_SB(0, 1), cB + hstep, voffB); PG8_STAGE(PG8_SA(0, 0), cA, voffA); PG8_STAGE(PG8_SA(0, 1), cA + hstep, voffA);
;         if (wr == 1) PG8_BAR;
;         PG8_WAIT_V(2); PG8_BAR;
.LBB0_143:
	s_nop 0
	v_writelane_b32 v255, s3, 26
	s_mul_i32 s3, s3, 10
	s_or_b32 s0, s3, 1
	s_cmp_le_i32 s86, s0
	s_cselect_b64 s[4:5], -1, 0
	s_cmp_lt_i32 s0, s87
	s_cselect_b64 s[18:19], -1, 0
	s_and_b64 s[4:5], s[4:5], s[18:19]
	s_add_i32 s78, s3, 2
	s_cmp_lt_i32 s78, s87
	v_writelane_b32 v255, s3, 27
	s_cselect_b64 s[24:25], -1, 0
	s_andn2_b64 vcc, exec, s[4:5]
	s_cbranch_vccnz .LBB0_276
	v_readlane_b32 s4, v250, 52
	s_waitcnt vmcnt(0)
	v_mov_b32_e32 v14, v234
	v_readlane_b32 s5, v250, 53
	s_andn2_b64 vcc, exec, s[4:5]
	v_readfirstlane_b32 s0, v14
	s_cbranch_vccnz .LBB0_181
	v_lshlrev_b32_e32 v1, 4, v14
	v_add_u32_e32 v2, 0x2000, v1
	s_waitcnt lgkmcnt(0)
	v_ashrrev_i32_e32 v4, 31, v2
	v_lshrrev_b32_e32 v4, 22, v4
	v_add_u32_e32 v4, v2, v4
	v_ashrrev_i32_e32 v8, 10, v4
	v_mul_i32_i24_e32 v4, 0x400, v8
	v_sub_u32_e32 v2, v2, v4
	v_lshrrev_b32_e32 v4, 4, v2
	v_bitop3_b32 v2, v4, v2, 32 bitop3:0x6c
	v_writelane_b32 v255, s24, 28
	v_ashrrev_i32_e32 v4, 31, v2
	v_lshrrev_b32_e32 v4, 26, v4
	v_writelane_b32 v255, s25, 29
	s_ashr_i32 s3, s0, 6
	v_readlane_b32 s31, v255, 26
	v_add_u32_e32 v4, v2, v4
	v_lshlrev_b32_e32 v5, 3, v8
	s_ashr_i32 s5, s0, 8
	s_lshl_b32 s4, s3, 10
	s_mul_i32 s16, s31, 0x1c00000
	v_readlane_b32 s18, v250, 26
	v_ashrrev_i32_e32 v9, 6, v4
	v_and_b32_e32 v5, -16, v5
	s_add_u32 s79, s18, s16
	v_readlane_b32 s16, v250, 27
	v_add_u32_e32 v5, v9, v5
	s_addc_u32 s80, s16, 0
	v_and_b32_e32 v6, 3, v9
	s_mov_b32 s16, 0x1fffe0
	v_lshrrev_b32_e32 v7, 2, v5
	v_lshlrev_b32_e32 v10, 1, v5
	v_and_b32_e32 v4, 0xc0, v4
	v_and_or_b32 v6, v5, s16, v6
	v_and_b32_e32 v7, 4, v7
	v_and_b32_e32 v10, 24, v10
	v_sub_u32_e32 v2, v2, v4
	v_or3_b32 v6, v6, v7, v10
	v_lshlrev_b32_e32 v7, 5, v8
	v_ashrrev_i16_sdwa v2, v235, sext(v2) dst_sel:DWORD dst_unused:UNUSED_PAD src0_sel:DWORD src1_sel:BYTE_0
	v_and_b32_e32 v7, 32, v7
	v_bfe_i32 v10, v2, 0, 16
	v_add_lshl_u32 v2, v7, v10, 1
	v_lshl_add_u32 v196, v6, 11, v2
	v_lshl_add_u32 v202, v5, 11, v2
	v_bfe_i32 v2, v14, 27, 1
	v_lshrrev_b32_e32 v2, 22, v2
	v_add_u32_e32 v2, v1, v2
	v_and_b32_e32 v2, 0xfffffc00, v2
	v_sub_u32_e32 v1, v1, v2
	v_lshrrev_b32_e32 v2, 4, v1
	v_ashrrev_i32_e32 v4, 31, v14
	v_bitop3_b32 v1, v2, v1, 32 bitop3:0x6c
	v_lshrrev_b32_e32 v4, 26, v4
	v_ashrrev_i32_e32 v2, 31, v1
	v_add_u32_e32 v4, v14, v4
	v_lshrrev_b32_e32 v2, 26, v2
	v_ashrrev_i32_e32 v12, 6, v4
	v_add_u32_e32 v2, v1, v2
	v_lshlrev_b32_e32 v4, 3, v12
	v_ashrrev_i32_e32 v11, 6, v2
	v_and_b32_e32 v4, -16, v4
	v_add_u32_e32 v4, v11, v4
	v_and_b32_e32 v5, 3, v11
	v_lshrrev_b32_e32 v6, 2, v4
	v_lshlrev_b32_e32 v7, 1, v4
	v_and_b32_e32 v2, 0xc0, v2
	v_and_or_b32 v5, v4, s16, v5
	v_and_b32_e32 v6, 4, v6
	v_and_b32_e32 v7, 24, v7
	v_sub_u32_e32 v1, v1, v2
	v_readlane_b32 s18, v253, 49
	v_or3_b32 v5, v5, v6, v7
	v_lshlrev_b32_e32 v6, 5, v12
	v_ashrrev_i16_sdwa v1, v235, sext(v1) dst_sel:DWORD dst_unused:UNUSED_PAD src0_sel:DWORD src1_sel:BYTE_0
	v_readlane_b32 s19, v253, 50
	s_add_u32 s38, s79, s18
	v_and_b32_e32 v6, 32, v6
	v_bfe_i32 v13, v1, 0, 16
	s_addc_u32 s39, s80, s19
	s_add_i32 s81, s4, 0
	v_add_lshl_u32 v1, v6, v13, 1
	s_add_i32 s18, s81, 0x10000
	s_add_i32 s19, s81, 0x12000
	v_lshl_add_u32 v2, v5, 11, v1
	s_mov_b32 m0, s18
	s_add_u32 s24, s38, 0x40000
	global_load_lds_dwordx4 v2, s[38:39]
	s_mov_b32 m0, s19
	s_addc_u32 s25, s39, 0
	s_add_i32 s16, s81, 0x14000
	global_load_lds_dwordx4 v196, s[38:39]
	s_mov_b32 m0, s16
	s_add_i32 s90, s81, 0x16000
	global_load_lds_dwordx4 v2, s[24:25]
	s_mov_b32 m0, s90
	v_lshl_add_u32 v204, v4, 11, v1
	global_load_lds_dwordx4 v196, s[24:25]
	v_readlane_b32 s24, v253, 57
	s_mov_b32 m0, s81
	v_readlane_b32 s25, v253, 58
	s_add_i32 s72, s81, 0x2000
	s_add_i32 s73, s81, 0x4000
	s_add_i32 s4, s81, 0x6000
	v_mov_b32_e32 v197, v3
	s_cmp_eq_u32 s5, 1
	global_load_lds_dwordx4 v204, s[24:25]
	s_mov_b32 m0, s72
	v_lshl_add_u64 v[4:5], s[38:39], 0, v[2:3]
	global_load_lds_dwordx4 v202, s[24:25]
	v_readlane_b32 s24, v253, 59
	s_mov_b32 m0, s73
	v_readlane_b32 s25, v253, 60
	s_cselect_b64 s[42:43], -1, 0
	s_cmp_lg_u32 s5, 1
	v_lshl_add_u64 v[6:7], s[38:39], 0, v[196:197]
	s_nop 1
	global_load_lds_dwordx4 v204, s[24:25]
	s_mov_b32 m0, s4
	s_nop 0
	global_load_lds_dwordx4 v202, s[24:25]
	s_cbranch_scc1 .LBB0_147
	s_barrier

; #define TS_BEG(sw, id) do { if ((id) == TSSEL && (sw).on) (sw).t0 = __builtin_amdgcn_s_memrealtime(); } while (0)
; #define TS_BEG(sw, id) do { } while (0)
; #define LTID() ({ int t_ = threadIdx.x; asm volatile("" : "+v"(t_)); t_; })
; #define SEAM(k) do { if (SINGLE_LAUNCH && IN(k) && IN((k) + 1)) { const int j_ = ((k) - 1 + NPH_LAYER) % NPH_LAYER; \
;         if (local_ok && (k) >= 1 && (j_ >= 4 || j_ == 1 || j_ == 2)) { xl_target += 32u; xl_barrier(bar.bar, bar.bar + XL_CNT(bar.x), xl_target); }        \
;         else if (local_ok && (k) >= 1) pair_barrier(bar.bar, bar.x);        \
;         else xcd_barrier(bar); } } while (0)
; __global__ void __launch_bounds__(NWAVES * 64, 2) fwd(Args args) {
;     ...
;         SEAM(pb + 0);
;         if (PHM(2) && IN(pb + 1)) for (int rep_ = 0; rep_ < REPS(2); ++rep_) {
;             const int tid = LTID(), lane = tid & 63;
;             TS_BEG(sw_, 70);
;             if (NAIVE & 1) naive_pool(lds, PROJ, pool_w + (size_t)l * 4 * 65536, pool_scale + l * MIXW, Y, vcu, G, tid);
;             else if (UEN(0)) for (int r2_ = 0; r2_ < REPS(11); ++r2_) for (int q_ = 0; q_ < 2; ++q_) { const int u = local_ok ? ((lvcu >> 6) * 128 + q_ * 64 + (lvcu & 63)) : (vcu + q_ * G); if (u >= 512) break; pool_unit(lds, PROJ, POOLT + (size_t)l * 4 * 65536, pool_scale + l * MIXW, Y, u >> 2, q_ ? 3 - (u & 3) : (u & 3), tid, lane, wave, sw_); }
.LBB0_276:
	s_nop 0
	s_cmp_le_i32 s86, s78
	s_cselect_b64 s[4:5], -1, 0
	v_readlane_b32 s0, v255, 27
	s_and_b64 s[4:5], s[4:5], s[24:25]
	s_add_i32 s0, s0, 3
	s_cmp_lt_i32 s0, s87
	v_writelane_b32 v255, s0, 30
	s_cselect_b64 s[18:19], -1, 0
	v_writelane_b32 v255, s18, 28
	s_andn2_b64 vcc, exec, s[4:5]
	s_nop 0
	v_writelane_b32 v255, s19, 29
	s_cbranch_vccnz .LBB0_523
	v_readlane_b32 s4, v255, 26
	s_lshl_b32 s0, s4, 19
	v_readlane_b32 s3, v250, 24
	s_add_u32 s36, s3, s0
	v_readlane_b32 s0, v250, 25
	s_addc_u32 s37, s0, 0
	s_lshl_b32 s34, s4, 10
	v_readlane_b32 s40, v250, 34
	s_lshl_b64 s[4:5], s[34:35], 2
	v_readlane_b32 s46, v250, 40
	v_readlane_b32 s47, v250, 41
	v_readlane_b32 s41, v250, 35
	v_readlane_b32 s48, v250, 42
	v_readlane_b32 s49, v250, 43
	v_readlane_b32 s50, v250, 44
	v_readlane_b32 s51, v250, 45
	v_readlane_b32 s46, v255, 22
	s_add_u32 s38, s40, s4
	v_readlane_b32 s47, v255, 23
	s_addc_u32 s39, s41, s5
	v_mov_b32_e32 v1, v234
	s_mov_b32 s0, 0
	s_mov_b64 s[40:41], -1
	v_readlane_b32 s24, v252, 10
	v_readlane_b32 s25, v252, 11
	v_readlane_b32 s31, v254, 27
	v_readlane_b32 s34, v252, 14
	v_readlane_b32 s48, v252, 15
	v_readlane_b32 s49, v252, 16
	v_readlane_b32 s50, v252, 17
	v_readlane_b32 s51, v252, 18
	v_readlane_b32 s42, v250, 36
	v_readlane_b32 s43, v250, 37
	v_readlane_b32 s44, v250, 38
	v_readlane_b32 s45, v250, 39
	v_readlane_b32 s52, v250, 46
	v_readlane_b32 s53, v250, 47
	v_readlane_b32 s54, v250, 48
	v_readlane_b32 s55, v250, 49
	s_branch .LBB0_280
